# layer-0 projector: first step peeled, its enc loads issued before the bias/Wih wait (one memory round trip less before recurrent step 0)
# baseline (speedup 1.0000x reference)
.LBB0_11:
	s_andn2_saveexec_b64 s[26:27], s[6:7]
	s_cbranch_execz .LBB0_32
	s_and_b32 s4, s2, -8
	v_lshrrev_b32_e32 v1, 2, v130
	v_and_or_b32 v34, v1, 4, s4
	s_lshl_b32 s4, s3, 5
	s_add_i32 s4, s4, s33
	s_ashr_i32 s5, s4, 31
	s_lshl_b64 s[6:7], s[4:5], 14
	s_add_u32 s6, s38, s6
	s_addc_u32 s7, s39, s7
	v_mov_b32_e32 v67, 0
	v_lshlrev_b32_e32 v66, 4, v130
	v_lshl_add_u64 v[46:47], s[6:7], 0, v[66:67]
	global_load_dwordx4 v[2:5], v66, s[6:7]
	global_load_dwordx4 v[6:9], v66, s[6:7] offset:1024
	global_load_dwordx4 v[10:13], v66, s[6:7] offset:2048
	global_load_dwordx4 v[14:17], v66, s[6:7] offset:3072
	s_movk_i32 s6, 0x1000
	v_add_co_u32_e32 v68, vcc, s6, v46
	s_movk_i32 s6, 0x2000
	s_nop 0
	v_addc_co_u32_e32 v69, vcc, 0, v47, vcc
	s_lshl_b32 s30, s3, 10
	s_lshl_b32 s28, s3, 12
	v_add_co_u32_e32 v48, vcc, s6, v46
	s_add_u32 s6, s44, s28
	v_ashrrev_i32_e32 v35, 31, v34
	s_addc_u32 s7, s45, 0
	v_lshlrev_b64 v[82:83], 2, v[34:35]
	v_lshl_add_u64 v[34:35], s[6:7], 0, v[82:83]
	s_add_u32 s6, s46, s28
	v_lshlrev_b32_e32 v131, 3, v0
	s_addc_u32 s7, s47, 0
	v_and_b32_e32 v84, 0x100, v131
	v_addc_co_u32_e32 v49, vcc, 0, v47, vcc
	v_lshl_add_u64 v[36:37], s[6:7], 0, v[82:83]
	v_lshlrev_b32_e32 v38, 2, v84
	v_mov_b32_e32 v39, v67
	s_movk_i32 s6, 0x3000
	v_lshl_add_u64 v[50:51], v[34:35], 0, v[38:39]
	v_lshl_add_u64 v[52:53], v[36:37], 0, v[38:39]
	v_add_co_u32_e32 v70, vcc, s6, v46
	global_load_dwordx4 v[18:21], v[68:69], off offset:1024
	global_load_dwordx4 v[22:25], v[68:69], off offset:2048
	global_load_dwordx4 v[26:29], v[48:49], off offset:-4096
	global_load_dwordx4 v[30:33], v[48:49], off
	global_load_dwordx4 v[74:77], v[50:51], off
	global_load_dwordx4 v[78:81], v[50:51], off offset:2048
	global_load_dwordx4 v[86:89], v[52:53], off
	global_load_dwordx4 v[90:93], v[52:53], off offset:2048
	global_load_dwordx4 v[34:37], v[48:49], off offset:1024
	global_load_dwordx4 v[38:41], v[48:49], off offset:2048
	global_load_dwordx4 v[42:45], v[48:49], off offset:3072
	v_addc_co_u32_e32 v71, vcc, 0, v47, vcc
	global_load_dwordx4 v[46:49], v[68:69], off offset:3072
	global_load_dwordx4 v[50:53], v[70:71], off
	global_load_dwordx4 v[54:57], v[70:71], off offset:1024
	global_load_dwordx4 v[58:61], v[70:71], off offset:2048
	global_load_dwordx4 v[62:65], v[70:71], off offset:3072
	v_mov_b32_e32 v69, 0xbfb8aa3b
	v_mov_b32_e32 v70, 0x4038aa3b
	v_cmp_gt_u32_e32 vcc, 32, v130
	v_lshrrev_b32_e32 v1, 6, v0
	s_mov_b32 s28, 0xbfb8aa3b
	v_cndmask_b32_e32 v132, v69, v70, vcc
	v_mov_b32_e32 v133, v132
	v_lshlrev_b32_e32 v71, 8, v0
	v_lshl_or_b32 v66, v1, 11, v66
	v_and_b32_e32 v68, 48, v130
	v_and_b32_e32 v85, 0xf00, v71
	v_mov_b32_e32 v69, v67
	v_lshl_add_u32 v72, v1, 2, 0
	v_add_u32_e32 v66, 0, v66
	s_cmp_eq_u32 s3, 0
	v_lshrrev_b32_e32 v136, 4, v130
	v_add_u32_e32 v70, -3, v1
	v_sub_u32_e32 v71, 30, v1
	v_mov_b32_e32 v134, v132
	v_mov_b32_e32 v135, v132
	v_lshl_add_u64 v[68:69], s[36:37], 0, v[68:69]
	v_add_u32_e32 v72, 0xeffc, v72
	s_cselect_b64 s[6:7], -1, 0
	v_add_u32_e32 v73, 0xfffff800, v66
	v_lshlrev_b32_e32 v128, 1, v85
	v_add_u32_e32 v70, 2, v70
	v_cndmask_b32_e64 v66, v71, v70, s[6:7]
	v_lshl_or_b32 v66, v66, 13, v128
	v_lshl_add_u64 v[118:119], v[68:69], 0, v[66:67]
	global_load_dwordx4 v[120:123], v[118:119], off
	global_load_dwordx4 v[124:127], v[118:119], off offset:64
	global_load_dwordx4 v[94:97], v[118:119], off offset:128
	global_load_dwordx4 v[98:101], v[118:119], off offset:192
	global_load_dwordx4 v[102:105], v[118:119], off offset:256
	global_load_dwordx4 v[106:109], v[118:119], off offset:320
	global_load_dwordx4 v[110:113], v[118:119], off offset:384
	global_load_dwordx4 v[114:117], v[118:119], off offset:448
	v_add_u32_e32 v71, -2, v71
	s_waitcnt vmcnt(17)
	v_pk_add_f32 v[74:75], v[74:75], v[86:87]
	v_pk_add_f32 v[76:77], v[76:77], v[88:89]
	s_waitcnt vmcnt(16)
	v_pk_add_f32 v[86:87], v[78:79], v[90:91]
	v_pk_add_f32 v[80:81], v[80:81], v[92:93]
	v_pk_mul_f32 v[78:79], v[76:77], s[28:29] op_sel_hi:[1,0]
	v_pk_mul_f32 v[76:77], v[74:75], s[28:29] op_sel_hi:[1,0]
	v_pk_mul_f32 v[86:87], v[132:133], v[86:87] op_sel_hi:[0,1]
	v_pk_mul_f32 v[88:89], v[132:133], v[80:81] op_sel_hi:[0,1]
	v_accvgpr_write_b32 a0, v76
	v_accvgpr_write_b32 a4, v86
	s_mov_b64 s[28:29], 0
	v_mov_b32_e32 v74, 1
	v_lshlrev_b32_e32 v75, 1, v85
	v_accvgpr_write_b32 a1, v77
	v_accvgpr_write_b32 a2, v78
	v_accvgpr_write_b32 a3, v79
	v_accvgpr_write_b32 a5, v87
	v_accvgpr_write_b32 a6, v88
	v_accvgpr_write_b32 a7, v89
	v_cmp_lt_u32_e32 vcc, 27, v70
	s_or_b64 s[28:29], vcc, s[28:29]
	s_waitcnt vmcnt(7)
	v_mfma_f32_16x16x32_f16 a[8:11], v[2:5], v[120:123], a[0:3]
	v_mfma_f32_16x16x32_f16 a[12:15], v[30:33], v[120:123], a[4:7]
	s_waitcnt vmcnt(6)
	v_mfma_f32_16x16x32_f16 a[8:11], v[6:9], v[124:127], a[8:11]
	v_mfma_f32_16x16x32_f16 a[12:15], v[34:37], v[124:127], a[12:15]
	s_waitcnt vmcnt(5)
	v_mfma_f32_16x16x32_f16 a[8:11], v[10:13], v[94:97], a[8:11]
	v_mfma_f32_16x16x32_f16 a[12:15], v[38:41], v[94:97], a[12:15]
	s_waitcnt vmcnt(4)
	v_mfma_f32_16x16x32_f16 a[8:11], v[14:17], v[98:101], a[8:11]
	v_mfma_f32_16x16x32_f16 a[12:15], v[42:45], v[98:101], a[12:15]
	s_waitcnt vmcnt(3)
	v_mfma_f32_16x16x32_f16 a[8:11], v[26:29], v[102:105], a[8:11]
	v_mfma_f32_16x16x32_f16 a[12:15], v[50:53], v[102:105], a[12:15]
	s_waitcnt vmcnt(2)
	v_mfma_f32_16x16x32_f16 a[8:11], v[18:21], v[106:109], a[8:11]
	v_mfma_f32_16x16x32_f16 a[12:15], v[54:57], v[106:109], a[12:15]
	s_waitcnt vmcnt(1)
	v_mfma_f32_16x16x32_f16 a[8:11], v[22:25], v[110:113], a[8:11]
	v_mfma_f32_16x16x32_f16 a[12:15], v[58:61], v[110:113], a[12:15]
	s_waitcnt vmcnt(0)
	v_mfma_f32_16x16x32_f16 a[8:11], v[46:49], v[114:117], a[8:11]
	v_mfma_f32_16x16x32_f16 a[12:15], v[62:65], v[114:117], a[12:15]
	s_nop 6
	ds_write_b128 v73, a[8:11]
	ds_write_b128 v73, a[12:15] offset:1024
	v_add_u32_e32 v73, 0x1000, v73
	ds_write_b32 v72, v74
	v_add_u32_e32 v72, 8, v72
	s_andn2_b64 exec, exec, s[28:29]
	s_cbranch_execz .Lp0_done

.Lp0_done:
	s_or_b64 exec, exec, s[28:29]
	s_lshl_b64 s[4:5], s[4:5], 15
	s_add_u32 s4, s40, s4
	s_addc_u32 s5, s41, s5
	v_lshlrev_b32_e32 v194, 4, v130
	v_mov_b32_e32 v195, 0
	v_lshl_add_u64 v[110:111], s[4:5], 0, v[194:195]
	global_load_dwordx4 v[2:5], v194, s[4:5]
	global_load_dwordx4 v[6:9], v194, s[4:5] offset:1024
	global_load_dwordx4 v[10:13], v194, s[4:5] offset:2048
	global_load_dwordx4 v[14:17], v194, s[4:5] offset:3072
	s_movk_i32 s4, 0x1000
	v_add_co_u32_e32 v86, vcc, s4, v110
	s_movk_i32 s4, 0x2000
	s_nop 0
	v_addc_co_u32_e32 v87, vcc, 0, v111, vcc
	v_add_co_u32_e32 v88, vcc, s4, v110
	s_movk_i32 s4, 0x3000
	s_nop 0
	v_addc_co_u32_e32 v89, vcc, 0, v111, vcc
	v_add_co_u32_e32 v90, vcc, s4, v110
	s_movk_i32 s4, 0x4000
	s_nop 0
	v_addc_co_u32_e32 v91, vcc, 0, v111, vcc
	v_add_co_u32_e32 v92, vcc, s4, v110
	s_movk_i32 s4, 0x5000
	s_nop 0
	v_addc_co_u32_e32 v93, vcc, 0, v111, vcc
	s_lshl_b32 s28, s30, 2
	v_add_co_u32_e32 v112, vcc, s4, v110
	s_add_u32 s4, s48, s28
	s_addc_u32 s5, s49, 0
	global_load_dwordx4 v[18:21], v[86:87], off offset:1024
	global_load_dwordx4 v[22:25], v[86:87], off offset:2048
	global_load_dwordx4 v[26:29], v[88:89], off offset:-4096
	global_load_dwordx4 v[30:33], v[88:89], off
	global_load_dwordx4 v[34:37], v[88:89], off offset:1024
	global_load_dwordx4 v[38:41], v[88:89], off offset:2048
	global_load_dwordx4 v[42:45], v[88:89], off offset:3072
	global_load_dwordx4 v[46:49], v[92:93], off offset:-4096
	global_load_dwordx4 v[50:53], v[86:87], off offset:3072
	global_load_dwordx4 v[54:57], v[90:91], off offset:1024
	global_load_dwordx4 v[58:61], v[90:91], off offset:2048
	global_load_dwordx4 v[62:65], v[90:91], off offset:3072
	global_load_dwordx4 v[66:69], v[92:93], off
	global_load_dwordx4 v[70:73], v[92:93], off offset:1024
	global_load_dwordx4 v[74:77], v[92:93], off offset:2048
	global_load_dwordx4 v[78:81], v[92:93], off offset:3072
	v_lshl_add_u64 v[86:87], s[4:5], 0, v[82:83]
	s_add_u32 s4, s50, s28
	s_addc_u32 s5, s51, 0
	v_addc_co_u32_e32 v113, vcc, 0, v111, vcc
	v_lshl_add_u64 v[82:83], s[4:5], 0, v[82:83]
	s_movk_i32 s4, 0x6000
	v_lshlrev_b32_e32 v194, 2, v84
	v_add_co_u32_e32 v106, vcc, s4, v110
	v_lshl_add_u64 v[84:85], v[86:87], 0, v[194:195]
	v_lshl_add_u64 v[82:83], v[82:83], 0, v[194:195]
	v_addc_co_u32_e32 v107, vcc, 0, v111, vcc
	s_movk_i32 s4, 0x7000
	global_load_dwordx4 v[138:141], v[84:85], off
	global_load_dwordx4 v[142:145], v[82:83], off
	global_load_dwordx4 v[146:149], v[84:85], off offset:2048
	global_load_dwordx4 v[150:153], v[82:83], off offset:2048
	s_nop 0
	global_load_dwordx4 v[82:85], v[112:113], off offset:1024
	global_load_dwordx4 v[86:89], v[112:113], off offset:2048
	global_load_dwordx4 v[90:93], v[106:107], off offset:-4096
	global_load_dwordx4 v[94:97], v[106:107], off
	global_load_dwordx4 v[98:101], v[106:107], off offset:1024
	global_load_dwordx4 v[102:105], v[106:107], off offset:2048
	s_nop 0
	global_load_dwordx4 v[106:109], v[106:107], off offset:3072
	v_add_co_u32_e32 v126, vcc, s4, v110
	s_mov_b32 s4, 0xbfb8aa3b
	s_nop 0
	v_addc_co_u32_e32 v127, vcc, 0, v111, vcc
	global_load_dwordx4 v[110:113], v[112:113], off offset:3072
	s_nop 0
	global_load_dwordx4 v[114:117], v[126:127], off
	global_load_dwordx4 v[118:121], v[126:127], off offset:1024
	global_load_dwordx4 v[122:125], v[126:127], off offset:2048
	s_nop 0
	global_load_dwordx4 v[126:129], v[126:127], off offset:3072
	v_add_u32_e32 v204, -1, v1
	v_lshl_add_u32 v1, v130, 4, 0
	v_and_b32_e32 v130, 0x78, v131
	v_lshl_or_b32 v205, v136, 7, v130
	v_or_b32_e32 v206, 0x1e000, v205
	s_mov_b64 s[28:29], 0
	s_mov_b64 s[30:31], 0x1000
	s_mov_b32 s40, 0xfffeffff
	v_mov_b32_e32 v207, 2
	s_waitcnt vmcnt(14)
	v_pk_add_f32 v[138:139], v[138:139], v[142:143]
	v_pk_add_f32 v[140:141], v[140:141], v[144:145]
	s_waitcnt vmcnt(12)
	v_pk_add_f32 v[142:143], v[146:147], v[150:151]
	v_pk_mul_f32 v[140:141], v[140:141], s[4:5] op_sel_hi:[1,0]
	v_pk_mul_f32 v[138:139], v[138:139], s[4:5] op_sel_hi:[1,0]
	v_pk_add_f32 v[144:145], v[148:149], v[152:153]
	v_pk_mul_f32 v[132:133], v[132:133], v[142:143]
	s_and_b64 s[4:5], s[6:7], exec
	v_pk_mul_f32 v[134:135], v[134:135], v[144:145]
	s_cselect_b32 s38, -8, -1
	s_cmp_eq_u32 s3, 1
	v_accvgpr_write_b32 a0, v138
	v_accvgpr_write_b32 a4, v132
	s_cselect_b32 s39, -8, -1
	v_cmp_eq_u32_e64 s[4:5], 0, v204
	v_accvgpr_write_b32 a1, v139
	v_accvgpr_write_b32 a2, v140
	v_accvgpr_write_b32 a3, v141
	v_accvgpr_write_b32 a5, v133
	v_accvgpr_write_b32 a6, v134
	v_accvgpr_write_b32 a7, v135
	s_branch .LBB0_16
